# cross attention softmax: half-wave max / sum exchange by v_permlane32_swap instead of ds_bpermute; redundant canonicalising max dropped
# baseline (speedup 1.0000x reference)
.LBB0_1221:
	v_mov_b64_e32 v[4:5], 0x200
	v_cmp_lt_i64_e32 vcc, s[4:5], v[4:5]
	s_mov_b64 s[4:5], -1
	s_cbranch_vccz .LBB0_1214
	v_readlane_b32 s7, v255, 58
	s_ashr_i32 s20, s7, 4
	v_readfirstlane_b32 s6, v173
	s_lshl_b32 s7, s7, 8
	s_ashr_i32 s21, s20, 31
	s_and_b32 s9, s7, 0xf00
	s_ashr_i32 s6, s6, 1
	s_lshl_b64 s[4:5], s[20:21], 12
	s_andn2_b32 s6, s6, 31
	v_or_b32_e32 v4, s9, v176
	s_ashr_i32 s7, s6, 31
	v_or_b32_e32 v4, s4, v4
	v_mov_b32_e32 v5, s5
	v_lshl_add_u64 v[4:5], v[4:5], 0, s[6:7]
	v_lshlrev_b64 v[6:7], 6, v[4:5]
	v_lshl_add_u64 v[18:19], s[14:15], 0, v[6:7]
	global_load_dwordx4 v[6:9], v[18:19], off offset:48
	global_load_dwordx4 v[10:13], v[18:19], off offset:32
	global_load_dwordx4 v[14:17], v[18:19], off offset:16
	s_nop 0
	global_load_dwordx4 v[18:21], v[18:19], off
	v_lshlrev_b64 v[170:171], 11, v[4:5]
	v_lshl_add_u64 v[4:5], s[10:11], 0, v[170:171]
	s_waitcnt vmcnt(2)
	v_add_f32_e32 v10, v10, v11
	v_add_f32_e32 v12, v12, v13
	s_waitcnt vmcnt(0)
	v_mov_b32_e32 v22, v19
	v_mov_b32_e32 v23, v20
	v_mov_b32_e32 v19, v21
	v_mov_b32_e32 v20, v15
	v_mov_b32_e32 v21, v16
	v_mov_b32_e32 v15, v17
	v_pk_add_f32 v[18:19], v[22:23], v[18:19]
	v_pk_add_f32 v[14:15], v[20:21], v[14:15]
	v_pk_add_f32 v[18:19], v[18:19], v[18:19] op_sel:[0,1] op_sel_hi:[1,0]
	v_pk_add_f32 v[14:15], v[14:15], v[14:15] op_sel:[0,1] op_sel_hi:[1,0]
	v_mov_b32_e32 v19, v6
	v_mov_b32_e32 v15, v7
	v_mov_b32_e32 v11, v8
	v_mov_b32_e32 v13, v9
	v_pk_add_f32 v[6:7], v[18:19], v[14:15]
	v_pk_add_f32 v[8:9], v[10:11], v[12:13]
	s_nop 0
	v_pk_add_f32 v[6:7], v[6:7], v[8:9]
	s_nop 0
	v_add_f32_e32 v6, v6, v7
	v_fmamk_f32 v6, v6, 0x3a800000, v1
	v_cmp_gt_f32_e32 vcc, s29, v6
	v_mul_f32_e32 v7, 0x4f800000, v6
	s_nop 0
	v_cndmask_b32_e32 v6, v6, v7, vcc
	v_sqrt_f32_e32 v7, v6
	s_nop 0
	v_add_u32_e32 v8, -1, v7
	v_fma_f32 v9, -v8, v7, v6
	v_cmp_ge_f32_e64 s[38:39], 0, v9
	v_add_u32_e32 v9, 1, v7
	s_nop 0
	v_cndmask_b32_e64 v8, v7, v8, s[38:39]
	v_fma_f32 v7, -v9, v7, v6
	v_cmp_lt_f32_e64 s[38:39], 0, v7
	s_nop 1
	v_cndmask_b32_e64 v7, v8, v9, s[38:39]
	v_mul_f32_e32 v8, 0x37800000, v7
	v_cndmask_b32_e32 v7, v7, v8, vcc
	v_cmp_class_f32_e32 vcc, v6, v248
	s_nop 1
	v_cndmask_b32_e32 v6, v7, v6, vcc
	v_div_scale_f32 v7, s[4:5], v6, v6, 1.0
	v_rcp_f32_e32 v8, v7
	v_readlane_b32 s4, v255, 57
	s_lshl_b32 s22, s4, 8
	s_ashr_i32 s23, s22, 31
	v_fma_f32 v9, -v7, v8, 1.0
	v_fmac_f32_e32 v8, v9, v8
	v_div_scale_f32 v9, vcc, 1.0, v6, 1.0
	v_mul_f32_e32 v10, v9, v8
	v_fma_f32 v11, -v7, v10, v9
	s_lshl_b32 s4, s20, 8
	v_fmac_f32_e32 v10, v11, v8
	s_lshl_b64 s[18:19], s[22:23], 1
	s_ashr_i32 s5, s4, 31
	v_fma_f32 v7, -v7, v10, v9
	v_lshl_add_u64 v[38:39], v[148:149], 0, s[18:19]
	s_lshl_b64 s[6:7], s[4:5], 11
	v_div_fmas_f32 v7, v7, v8, v10
	v_lshl_add_u64 v[18:19], v[38:39], 0, s[6:7]
	v_div_fixup_f32 v42, v7, v6, 1.0
	v_lshl_add_u64 v[6:7], v[18:19], 0, v[150:151]
	s_or_b32 s6, s4, 64
	global_load_dwordx4 v[6:9], v[6:7], off
	v_lshl_add_u64 v[10:11], v[18:19], 0, v[152:153]
	s_ashr_i32 s7, s6, 31
	global_load_dwordx4 v[10:13], v[10:11], off
	v_lshl_add_u64 v[14:15], v[18:19], 0, v[154:155]
	s_lshl_b64 s[6:7], s[6:7], 11
	global_load_dwordx4 v[14:17], v[14:15], off
	v_lshl_add_u64 v[18:19], v[18:19], 0, v[156:157]
	v_lshl_add_u64 v[34:35], v[38:39], 0, s[6:7]
	global_load_dwordx4 v[18:21], v[18:19], off
	v_lshl_add_u64 v[22:23], v[34:35], 0, v[150:151]
	global_load_dwordx4 v[22:25], v[22:23], off
	v_lshl_add_u64 v[26:27], v[34:35], 0, v[152:153]
	global_load_dwordx4 v[26:29], v[26:27], off
	v_lshl_add_u64 v[30:31], v[34:35], 0, v[154:155]
	global_load_dwordx4 v[30:33], v[30:31], off
	v_lshl_add_u64 v[34:35], v[34:35], 0, v[156:157]
	global_load_dwordx4 v[34:37], v[34:35], off
	s_or_b32 s6, s4, 0x80
	s_ashr_i32 s7, s6, 31
	s_lshl_b64 s[6:7], s[6:7], 11
	v_lshl_add_u64 v[40:41], v[4:5], 0, s[18:19]
	s_or_b32 s4, s4, 0xc0
	s_ashr_i32 s5, s4, 31
	s_lshl_b64 s[4:5], s[4:5], 11
	v_lshl_add_u64 v[174:175], v[40:41], 0, v[2:3]
	v_mul_f32_e32 v172, 0x3db8aa3b, v42
	s_waitcnt vmcnt(7)
	ds_write_b128 v179, v[6:9]
	s_waitcnt vmcnt(6)
	ds_write_b128 v179, v[10:13] offset:8448
	s_waitcnt vmcnt(5)
	ds_write_b128 v179, v[14:17] offset:16896
	s_waitcnt vmcnt(4)
	ds_write_b128 v179, v[18:21] offset:25344
	s_waitcnt vmcnt(3)
	ds_write_b128 v179, v[22:25] offset:33792
	s_waitcnt vmcnt(2)
	ds_write_b128 v179, v[26:29] offset:42240
	s_waitcnt vmcnt(1)
	ds_write_b128 v179, v[30:33] offset:50688
	s_waitcnt vmcnt(0)
	ds_write_b128 v179, v[34:37] offset:59136
	v_lshl_add_u64 v[16:17], v[38:39], 0, s[6:7]
	v_lshl_add_u64 v[4:5], v[16:17], 0, v[150:151]
	global_load_dwordx4 v[4:7], v[4:5], off
	v_lshl_add_u64 v[8:9], v[16:17], 0, v[152:153]
	global_load_dwordx4 v[8:11], v[8:9], off
	v_lshl_add_u64 v[12:13], v[16:17], 0, v[154:155]
	global_load_dwordx4 v[12:15], v[12:13], off
	v_lshl_add_u64 v[16:17], v[16:17], 0, v[156:157]
	v_lshl_add_u64 v[32:33], v[38:39], 0, s[4:5]
	global_load_dwordx4 v[16:19], v[16:17], off
	v_lshl_add_u64 v[20:21], v[32:33], 0, v[150:151]
	global_load_dwordx4 v[20:23], v[20:21], off
	v_lshl_add_u64 v[24:25], v[32:33], 0, v[152:153]
	global_load_dwordx4 v[24:27], v[24:25], off
	v_lshl_add_u64 v[28:29], v[32:33], 0, v[154:155]
	global_load_dwordx4 v[28:31], v[28:29], off
	v_lshl_add_u64 v[32:33], v[32:33], 0, v[156:157]
	global_load_dwordx4 v[32:35], v[32:33], off
	s_lshl_b32 s4, s20, 10
	s_add_i32 s4, s22, s4
	s_ashr_i32 s5, s4, 31
	s_lshl_b64 s[12:13], s[4:5], 9
	s_mov_b32 s6, 0
	s_waitcnt vmcnt(7)
	ds_write_b128 v180, v[4:7]
	s_waitcnt vmcnt(6)
	ds_write_b128 v180, v[8:11] offset:8448
	s_waitcnt vmcnt(5)
	ds_write_b128 v180, v[12:15] offset:16896
	s_waitcnt vmcnt(4)
	ds_write_b128 v180, v[16:19] offset:25344
	s_waitcnt vmcnt(3)
	ds_write_b128 v181, v[20:23]
	s_waitcnt vmcnt(2)
	ds_write_b128 v181, v[24:27] offset:8448
	s_waitcnt vmcnt(1)
	ds_write_b128 v181, v[28:31] offset:16896
	s_waitcnt vmcnt(0)
	ds_write_b128 v181, v[32:35] offset:25344
	s_waitcnt lgkmcnt(0)
	s_barrier
	global_load_dwordx4 v[4:7], v[174:175], off
	global_load_dwordx4 v[140:143], v[174:175], off offset:32
	global_load_dwordx4 v[136:139], v[174:175], off offset:64
	global_load_dwordx4 v[132:135], v[174:175], off offset:96
	ds_read_b128 v[8:11], v177
	ds_read_b128 v[12:15], v177 offset:32
	s_waitcnt vmcnt(3) lgkmcnt(1)
	v_mfma_f32_32x32x16_bf16 v[116:131], v[8:11], v[4:7], 0
	ds_read_b128 v[8:11], v177 offset:64
	s_waitcnt vmcnt(2) lgkmcnt(1)
	v_mfma_f32_32x32x16_bf16 v[116:131], v[12:15], v[140:143], v[116:131]
	s_waitcnt vmcnt(1) lgkmcnt(0)
	v_mfma_f32_32x32x16_bf16 v[116:131], v[8:11], v[136:139], v[116:131]
	ds_read_b128 v[8:11], v177 offset:96
	s_waitcnt vmcnt(0) lgkmcnt(0)
	v_mfma_f32_32x32x16_bf16 v[116:131], v[8:11], v[132:135], v[116:131]
	ds_read_b128 v[8:11], v177 offset:16896
	s_waitcnt lgkmcnt(0)
	v_mfma_f32_32x32x16_bf16 v[100:115], v[8:11], v[4:7], 0
	ds_read_b128 v[8:11], v177 offset:16928
	s_waitcnt lgkmcnt(0)
	v_mfma_f32_32x32x16_bf16 v[100:115], v[8:11], v[140:143], v[100:115]
	ds_read_b128 v[8:11], v177 offset:16960
	s_waitcnt lgkmcnt(0)
	v_mfma_f32_32x32x16_bf16 v[100:115], v[8:11], v[136:139], v[100:115]
	ds_read_b128 v[8:11], v177 offset:16992
	s_waitcnt lgkmcnt(0)
	v_mfma_f32_32x32x16_bf16 v[100:115], v[8:11], v[132:135], v[100:115]
	ds_read_b128 v[8:11], v177 offset:33792
	s_waitcnt lgkmcnt(0)
	v_mfma_f32_32x32x16_bf16 v[84:99], v[8:11], v[4:7], 0
	ds_read_b128 v[8:11], v177 offset:33824
	s_waitcnt lgkmcnt(0)
	v_mfma_f32_32x32x16_bf16 v[84:99], v[8:11], v[140:143], v[84:99]
	ds_read_b128 v[8:11], v177 offset:33856
	s_waitcnt lgkmcnt(0)
	v_mfma_f32_32x32x16_bf16 v[84:99], v[8:11], v[136:139], v[84:99]
	ds_read_b128 v[8:11], v177 offset:33888
	s_waitcnt lgkmcnt(0)
	v_mfma_f32_32x32x16_bf16 v[84:99], v[8:11], v[132:135], v[84:99]
	ds_read_b128 v[8:11], v177 offset:50688
	s_waitcnt lgkmcnt(0)
	v_mfma_f32_32x32x16_bf16 v[68:83], v[8:11], v[4:7], 0
	ds_read_b128 v[8:11], v177 offset:50720
	s_waitcnt lgkmcnt(0)
	v_mfma_f32_32x32x16_bf16 v[68:83], v[8:11], v[140:143], v[68:83]
	ds_read_b128 v[8:11], v177 offset:50752
	s_waitcnt lgkmcnt(0)
	v_mfma_f32_32x32x16_bf16 v[68:83], v[8:11], v[136:139], v[68:83]
	ds_read_b128 v[8:11], v177 offset:50784
	s_waitcnt lgkmcnt(0)
	v_mfma_f32_32x32x16_bf16 v[68:83], v[8:11], v[132:135], v[68:83]
	ds_read_b128 v[8:11], v182
	ds_read_b128 v[12:15], v182 offset:32
	s_waitcnt lgkmcnt(1)
	v_mfma_f32_32x32x16_bf16 v[52:67], v[8:11], v[4:7], 0
	ds_read_b128 v[8:11], v182 offset:64
	s_waitcnt lgkmcnt(1)
	v_mfma_f32_32x32x16_bf16 v[52:67], v[12:15], v[140:143], v[52:67]
	s_waitcnt lgkmcnt(0)
	v_mfma_f32_32x32x16_bf16 v[52:67], v[8:11], v[136:139], v[52:67]
	ds_read_b128 v[8:11], v182 offset:96
	s_waitcnt lgkmcnt(0)
	v_mfma_f32_32x32x16_bf16 v[52:67], v[8:11], v[132:135], v[52:67]
	ds_read_b128 v[8:11], v183
	s_waitcnt lgkmcnt(0)
	v_mfma_f32_32x32x16_bf16 v[36:51], v[8:11], v[4:7], 0
	ds_read_b128 v[8:11], v183 offset:32
	s_waitcnt lgkmcnt(0)
	v_mfma_f32_32x32x16_bf16 v[36:51], v[8:11], v[140:143], v[36:51]
	ds_read_b128 v[8:11], v183 offset:64
	s_waitcnt lgkmcnt(0)
	v_mfma_f32_32x32x16_bf16 v[36:51], v[8:11], v[136:139], v[36:51]
	ds_read_b128 v[8:11], v183 offset:96
	s_waitcnt lgkmcnt(0)
	v_mfma_f32_32x32x16_bf16 v[36:51], v[8:11], v[132:135], v[36:51]
	ds_read_b128 v[8:11], v184
	ds_read_b128 v[12:15], v184 offset:32
	ds_read_b128 v[144:147], v185 offset:32
	s_waitcnt lgkmcnt(2)
	v_mfma_f32_32x32x16_bf16 v[20:35], v[8:11], v[4:7], 0
	ds_read_b128 v[8:11], v184 offset:64
	s_waitcnt lgkmcnt(2)
	v_mfma_f32_32x32x16_bf16 v[20:35], v[12:15], v[140:143], v[20:35]
	s_waitcnt lgkmcnt(0)
	v_mfma_f32_32x32x16_bf16 v[20:35], v[8:11], v[136:139], v[20:35]
	ds_read_b128 v[8:11], v184 offset:96
	s_waitcnt lgkmcnt(0)
	v_mfma_f32_32x32x16_bf16 v[20:35], v[8:11], v[132:135], v[20:35]
	ds_read_b128 v[8:11], v185
	s_waitcnt lgkmcnt(0)
	v_mfma_f32_32x32x16_bf16 v[4:19], v[8:11], v[4:7], 0
	v_mfma_f32_32x32x16_bf16 v[4:19], v[144:147], v[140:143], v[4:19]
	ds_read_b128 v[140:143], v185 offset:64
	s_waitcnt lgkmcnt(0)
	v_mfma_f32_32x32x16_bf16 v[4:19], v[140:143], v[136:139], v[4:19]
	ds_read_b128 v[136:139], v185 offset:96
	s_waitcnt lgkmcnt(0)
	v_mfma_f32_32x32x16_bf16 v[4:19], v[136:139], v[132:135], v[4:19]
	global_load_dwordx4 v[132:135], v[174:175], off offset:128
	global_load_dwordx4 v[136:139], v[174:175], off offset:160
	global_load_dwordx4 v[140:143], v[174:175], off offset:192
	global_load_dwordx4 v[144:147], v[174:175], off offset:224
	ds_read_b128 v[188:191], v177 offset:128
	s_waitcnt vmcnt(3) lgkmcnt(0)
	v_mfma_f32_32x32x16_bf16 v[116:131], v[188:191], v[132:135], v[116:131]
	ds_read_b128 v[188:191], v177 offset:160
	s_waitcnt vmcnt(2) lgkmcnt(0)
	v_mfma_f32_32x32x16_bf16 v[116:131], v[188:191], v[136:139], v[116:131]
	ds_read_b128 v[188:191], v177 offset:192
	s_waitcnt vmcnt(1) lgkmcnt(0)
	v_mfma_f32_32x32x16_bf16 v[116:131], v[188:191], v[140:143], v[116:131]
	ds_read_b128 v[188:191], v177 offset:224
	s_waitcnt vmcnt(0) lgkmcnt(0)
	v_mfma_f32_32x32x16_bf16 v[116:131], v[188:191], v[144:147], v[116:131]
	ds_read_b128 v[188:191], v177 offset:17024
	s_waitcnt lgkmcnt(0)
	v_mfma_f32_32x32x16_bf16 v[100:115], v[188:191], v[132:135], v[100:115]
	ds_read_b128 v[188:191], v177 offset:17056
	s_waitcnt lgkmcnt(0)
	v_mfma_f32_32x32x16_bf16 v[100:115], v[188:191], v[136:139], v[100:115]
	ds_read_b128 v[188:191], v177 offset:17088
	s_waitcnt lgkmcnt(0)
	v_mfma_f32_32x32x16_bf16 v[100:115], v[188:191], v[140:143], v[100:115]
	ds_read_b128 v[188:191], v177 offset:17120
	s_waitcnt lgkmcnt(0)
	v_mfma_f32_32x32x16_bf16 v[100:115], v[188:191], v[144:147], v[100:115]
	ds_read_b128 v[188:191], v177 offset:33920
	s_waitcnt lgkmcnt(0)
	v_mfma_f32_32x32x16_bf16 v[84:99], v[188:191], v[132:135], v[84:99]
	ds_read_b128 v[188:191], v177 offset:33952
	s_waitcnt lgkmcnt(0)
	v_mfma_f32_32x32x16_bf16 v[84:99], v[188:191], v[136:139], v[84:99]
	ds_read_b128 v[188:191], v177 offset:33984
	s_waitcnt lgkmcnt(0)
	v_mfma_f32_32x32x16_bf16 v[84:99], v[188:191], v[140:143], v[84:99]
	ds_read_b128 v[188:191], v177 offset:34016
	s_waitcnt lgkmcnt(0)
	v_mfma_f32_32x32x16_bf16 v[84:99], v[188:191], v[144:147], v[84:99]
	ds_read_b128 v[188:191], v177 offset:50816
	s_waitcnt lgkmcnt(0)
	v_mfma_f32_32x32x16_bf16 v[68:83], v[188:191], v[132:135], v[68:83]
	ds_read_b128 v[188:191], v177 offset:50848
	s_waitcnt lgkmcnt(0)
	v_mfma_f32_32x32x16_bf16 v[68:83], v[188:191], v[136:139], v[68:83]
	ds_read_b128 v[188:191], v177 offset:50880
	s_waitcnt lgkmcnt(0)
	v_mfma_f32_32x32x16_bf16 v[68:83], v[188:191], v[140:143], v[68:83]
	ds_read_b128 v[188:191], v177 offset:50912
	s_waitcnt lgkmcnt(0)
	v_mfma_f32_32x32x16_bf16 v[68:83], v[188:191], v[144:147], v[68:83]
	ds_read_b128 v[188:191], v182 offset:128
	s_waitcnt lgkmcnt(0)
	v_mfma_f32_32x32x16_bf16 v[52:67], v[188:191], v[132:135], v[52:67]
	ds_read_b128 v[188:191], v182 offset:160
	s_waitcnt lgkmcnt(0)
	v_mfma_f32_32x32x16_bf16 v[52:67], v[188:191], v[136:139], v[52:67]
	ds_read_b128 v[188:191], v182 offset:192
	s_waitcnt lgkmcnt(0)
	v_mfma_f32_32x32x16_bf16 v[52:67], v[188:191], v[140:143], v[52:67]
	ds_read_b128 v[188:191], v182 offset:224
	s_waitcnt lgkmcnt(0)
	v_mfma_f32_32x32x16_bf16 v[52:67], v[188:191], v[144:147], v[52:67]
	ds_read_b128 v[188:191], v186 offset:128
	ds_read_b128 v[192:195], v186 offset:160
	s_waitcnt lgkmcnt(1)
	v_mfma_f32_32x32x16_bf16 v[36:51], v[188:191], v[132:135], v[36:51]
	ds_read_b128 v[188:191], v186 offset:192
	s_waitcnt lgkmcnt(1)
	v_mfma_f32_32x32x16_bf16 v[36:51], v[192:195], v[136:139], v[36:51]
	s_waitcnt lgkmcnt(0)
	v_mfma_f32_32x32x16_bf16 v[36:51], v[188:191], v[140:143], v[36:51]
	ds_read_b128 v[188:191], v186 offset:224
	s_waitcnt lgkmcnt(0)
	v_mfma_f32_32x32x16_bf16 v[36:51], v[188:191], v[144:147], v[36:51]
	ds_read_b128 v[188:191], v184 offset:128
	s_waitcnt lgkmcnt(0)
	v_mfma_f32_32x32x16_bf16 v[20:35], v[188:191], v[132:135], v[20:35]
	ds_read_b128 v[188:191], v184 offset:160
	s_waitcnt lgkmcnt(0)
	v_mfma_f32_32x32x16_bf16 v[20:35], v[188:191], v[136:139], v[20:35]
	ds_read_b128 v[188:191], v184 offset:192
	s_waitcnt lgkmcnt(0)
	v_mfma_f32_32x32x16_bf16 v[20:35], v[188:191], v[140:143], v[20:35]
	ds_read_b128 v[188:191], v184 offset:224
	s_waitcnt lgkmcnt(0)
	v_mfma_f32_32x32x16_bf16 v[20:35], v[188:191], v[144:147], v[20:35]
	ds_read_b128 v[188:191], v187 offset:128
	ds_read_b128 v[192:195], v187 offset:160
	s_waitcnt lgkmcnt(1)
	v_mfma_f32_32x32x16_bf16 v[4:19], v[188:191], v[132:135], v[4:19]
	ds_read_b128 v[132:135], v187 offset:192
	s_waitcnt lgkmcnt(1)
	v_mfma_f32_32x32x16_bf16 v[4:19], v[192:195], v[136:139], v[4:19]
	s_waitcnt lgkmcnt(0)
	v_mfma_f32_32x32x16_bf16 v[4:19], v[132:135], v[140:143], v[4:19]
	ds_read_b128 v[132:135], v187 offset:224
	s_waitcnt lgkmcnt(0)
	v_mfma_f32_32x32x16_bf16 v[4:19], v[132:135], v[144:147], v[4:19]
	global_load_dwordx4 v[132:135], v[174:175], off offset:256
	global_load_dwordx4 v[136:139], v[174:175], off offset:288
	global_load_dwordx4 v[140:143], v[174:175], off offset:320
	global_load_dwordx4 v[144:147], v[174:175], off offset:352
	ds_read_b128 v[188:191], v177 offset:256
	s_waitcnt vmcnt(3) lgkmcnt(0)
	v_mfma_f32_32x32x16_bf16 v[116:131], v[188:191], v[132:135], v[116:131]
	ds_read_b128 v[188:191], v177 offset:288
	s_waitcnt vmcnt(2) lgkmcnt(0)
	v_mfma_f32_32x32x16_bf16 v[116:131], v[188:191], v[136:139], v[116:131]
	ds_read_b128 v[188:191], v177 offset:320
	s_waitcnt vmcnt(1) lgkmcnt(0)
	v_mfma_f32_32x32x16_bf16 v[116:131], v[188:191], v[140:143], v[116:131]
	ds_read_b128 v[188:191], v177 offset:352
	s_waitcnt vmcnt(0) lgkmcnt(0)
	v_mfma_f32_32x32x16_bf16 v[116:131], v[188:191], v[144:147], v[116:131]
	ds_read_b128 v[188:191], v177 offset:17152
	s_waitcnt lgkmcnt(0)
	v_mfma_f32_32x32x16_bf16 v[100:115], v[188:191], v[132:135], v[100:115]
	ds_read_b128 v[188:191], v177 offset:17184
	s_waitcnt lgkmcnt(0)
	v_mfma_f32_32x32x16_bf16 v[100:115], v[188:191], v[136:139], v[100:115]
	ds_read_b128 v[188:191], v177 offset:17216
	s_waitcnt lgkmcnt(0)
	v_mfma_f32_32x32x16_bf16 v[100:115], v[188:191], v[140:143], v[100:115]
	ds_read_b128 v[188:191], v177 offset:17248
	s_waitcnt lgkmcnt(0)
	v_mfma_f32_32x32x16_bf16 v[100:115], v[188:191], v[144:147], v[100:115]
	ds_read_b128 v[188:191], v177 offset:34048
	s_waitcnt lgkmcnt(0)
	v_mfma_f32_32x32x16_bf16 v[84:99], v[188:191], v[132:135], v[84:99]
	ds_read_b128 v[188:191], v177 offset:34080
	s_waitcnt lgkmcnt(0)
	v_mfma_f32_32x32x16_bf16 v[84:99], v[188:191], v[136:139], v[84:99]
	ds_read_b128 v[188:191], v177 offset:34112
	s_waitcnt lgkmcnt(0)
	v_mfma_f32_32x32x16_bf16 v[84:99], v[188:191], v[140:143], v[84:99]
	ds_read_b128 v[188:191], v177 offset:34144
	s_waitcnt lgkmcnt(0)
	v_mfma_f32_32x32x16_bf16 v[84:99], v[188:191], v[144:147], v[84:99]
	ds_read_b128 v[188:191], v177 offset:50944
	s_waitcnt lgkmcnt(0)
	v_mfma_f32_32x32x16_bf16 v[68:83], v[188:191], v[132:135], v[68:83]
	ds_read_b128 v[188:191], v177 offset:50976
	s_waitcnt lgkmcnt(0)
	v_mfma_f32_32x32x16_bf16 v[68:83], v[188:191], v[136:139], v[68:83]
	ds_read_b128 v[188:191], v177 offset:51008
	s_waitcnt lgkmcnt(0)
	v_mfma_f32_32x32x16_bf16 v[68:83], v[188:191], v[140:143], v[68:83]
	ds_read_b128 v[188:191], v177 offset:51040
	s_waitcnt lgkmcnt(0)
	v_mfma_f32_32x32x16_bf16 v[68:83], v[188:191], v[144:147], v[68:83]
	ds_read_b128 v[188:191], v182 offset:256
	s_waitcnt lgkmcnt(0)
	v_mfma_f32_32x32x16_bf16 v[52:67], v[188:191], v[132:135], v[52:67]
	ds_read_b128 v[188:191], v182 offset:288
	s_waitcnt lgkmcnt(0)
	v_mfma_f32_32x32x16_bf16 v[52:67], v[188:191], v[136:139], v[52:67]
	ds_read_b128 v[188:191], v182 offset:320
	s_waitcnt lgkmcnt(0)
	v_mfma_f32_32x32x16_bf16 v[52:67], v[188:191], v[140:143], v[52:67]
	ds_read_b128 v[188:191], v182 offset:352
	s_waitcnt lgkmcnt(0)
	v_mfma_f32_32x32x16_bf16 v[52:67], v[188:191], v[144:147], v[52:67]
	ds_read_b128 v[188:191], v186 offset:256
	s_waitcnt lgkmcnt(0)
	v_mfma_f32_32x32x16_bf16 v[36:51], v[188:191], v[132:135], v[36:51]
	ds_read_b128 v[188:191], v186 offset:288
	s_waitcnt lgkmcnt(0)
	v_mfma_f32_32x32x16_bf16 v[36:51], v[188:191], v[136:139], v[36:51]
	ds_read_b128 v[188:191], v186 offset:320
	s_waitcnt lgkmcnt(0)
	v_mfma_f32_32x32x16_bf16 v[36:51], v[188:191], v[140:143], v[36:51]
	ds_read_b128 v[188:191], v186 offset:352
	s_waitcnt lgkmcnt(0)
	v_mfma_f32_32x32x16_bf16 v[36:51], v[188:191], v[144:147], v[36:51]
	ds_read_b128 v[188:191], v184 offset:256
	s_waitcnt lgkmcnt(0)
	v_mfma_f32_32x32x16_bf16 v[20:35], v[188:191], v[132:135], v[20:35]
	ds_read_b128 v[188:191], v184 offset:288
	s_waitcnt lgkmcnt(0)
	v_mfma_f32_32x32x16_bf16 v[20:35], v[188:191], v[136:139], v[20:35]
	ds_read_b128 v[188:191], v184 offset:320
	s_waitcnt lgkmcnt(0)
	v_mfma_f32_32x32x16_bf16 v[20:35], v[188:191], v[140:143], v[20:35]
	ds_read_b128 v[188:191], v184 offset:352
	s_waitcnt lgkmcnt(0)
	v_mfma_f32_32x32x16_bf16 v[20:35], v[188:191], v[144:147], v[20:35]
	ds_read_b128 v[188:191], v187 offset:256
	s_waitcnt lgkmcnt(0)
	v_mfma_f32_32x32x16_bf16 v[4:19], v[188:191], v[132:135], v[4:19]
	ds_read_b128 v[132:135], v187 offset:288
	s_waitcnt lgkmcnt(0)
	v_mfma_f32_32x32x16_bf16 v[4:19], v[132:135], v[136:139], v[4:19]
	ds_read_b128 v[132:135], v187 offset:320
	s_waitcnt lgkmcnt(0)
	v_mfma_f32_32x32x16_bf16 v[4:19], v[132:135], v[140:143], v[4:19]
	ds_read_b128 v[132:135], v187 offset:352
	s_waitcnt lgkmcnt(0)
	v_mfma_f32_32x32x16_bf16 v[4:19], v[132:135], v[144:147], v[4:19]
	global_load_dwordx4 v[136:139], v[174:175], off offset:384
	global_load_dwordx4 v[144:147], v[174:175], off offset:416
	global_load_dwordx4 v[140:143], v[174:175], off offset:448
	global_load_dwordx4 v[132:135], v[174:175], off offset:480
	ds_read_b128 v[188:191], v177 offset:384
	s_waitcnt vmcnt(3) lgkmcnt(0)
	v_mfma_f32_32x32x16_bf16 v[116:131], v[188:191], v[136:139], v[116:131]
	ds_read_b128 v[188:191], v177 offset:416
	s_waitcnt vmcnt(2) lgkmcnt(0)
	v_mfma_f32_32x32x16_bf16 v[116:131], v[188:191], v[144:147], v[116:131]
	ds_read_b128 v[188:191], v177 offset:448
	s_waitcnt vmcnt(1) lgkmcnt(0)
	v_mfma_f32_32x32x16_bf16 v[116:131], v[188:191], v[140:143], v[116:131]
	ds_read_b128 v[188:191], v177 offset:480
	s_waitcnt vmcnt(0) lgkmcnt(0)
	v_mfma_f32_32x32x16_bf16 v[116:131], v[188:191], v[132:135], v[116:131]
	ds_read_b128 v[188:191], v177 offset:17280
	s_waitcnt lgkmcnt(0)
	v_mfma_f32_32x32x16_bf16 v[100:115], v[188:191], v[136:139], v[100:115]
	ds_read_b128 v[188:191], v177 offset:17312
	s_waitcnt lgkmcnt(0)
	v_mfma_f32_32x32x16_bf16 v[100:115], v[188:191], v[144:147], v[100:115]
	ds_read_b128 v[188:191], v177 offset:17344
	s_waitcnt lgkmcnt(0)
	v_mfma_f32_32x32x16_bf16 v[100:115], v[188:191], v[140:143], v[100:115]
	ds_read_b128 v[188:191], v177 offset:17376
	s_waitcnt lgkmcnt(0)
	v_mfma_f32_32x32x16_bf16 v[100:115], v[188:191], v[132:135], v[100:115]
	ds_read_b128 v[188:191], v177 offset:34176
	s_waitcnt lgkmcnt(0)
	v_mfma_f32_32x32x16_bf16 v[84:99], v[188:191], v[136:139], v[84:99]
	ds_read_b128 v[188:191], v177 offset:34208
	s_waitcnt lgkmcnt(0)
	v_mfma_f32_32x32x16_bf16 v[84:99], v[188:191], v[144:147], v[84:99]
	ds_read_b128 v[188:191], v177 offset:34240
	s_waitcnt lgkmcnt(0)
	v_mfma_f32_32x32x16_bf16 v[84:99], v[188:191], v[140:143], v[84:99]
	ds_read_b128 v[188:191], v177 offset:34272
	s_waitcnt lgkmcnt(0)
	v_mfma_f32_32x32x16_bf16 v[84:99], v[188:191], v[132:135], v[84:99]
	ds_read_b128 v[188:191], v177 offset:51072
	s_waitcnt lgkmcnt(0)
	v_mfma_f32_32x32x16_bf16 v[68:83], v[188:191], v[136:139], v[68:83]
	ds_read_b128 v[188:191], v177 offset:51104
	s_waitcnt lgkmcnt(0)
	v_mfma_f32_32x32x16_bf16 v[68:83], v[188:191], v[144:147], v[68:83]
	ds_read_b128 v[188:191], v177 offset:51136
	s_waitcnt lgkmcnt(0)
	v_mfma_f32_32x32x16_bf16 v[68:83], v[188:191], v[140:143], v[68:83]
	ds_read_b128 v[188:191], v177 offset:51168
	s_waitcnt lgkmcnt(0)
	v_mfma_f32_32x32x16_bf16 v[68:83], v[188:191], v[132:135], v[68:83]
	ds_read_b128 v[188:191], v182 offset:384
	s_waitcnt lgkmcnt(0)
	v_mfma_f32_32x32x16_bf16 v[52:67], v[188:191], v[136:139], v[52:67]
	ds_read_b128 v[188:191], v182 offset:416
	s_waitcnt lgkmcnt(0)
	v_mfma_f32_32x32x16_bf16 v[52:67], v[188:191], v[144:147], v[52:67]
	ds_read_b128 v[188:191], v182 offset:448
	s_waitcnt lgkmcnt(0)
	v_mfma_f32_32x32x16_bf16 v[52:67], v[188:191], v[140:143], v[52:67]
	ds_read_b128 v[188:191], v182 offset:480
	s_waitcnt lgkmcnt(0)
	v_mfma_f32_32x32x16_bf16 v[52:67], v[188:191], v[132:135], v[52:67]
	ds_read_b128 v[188:191], v186 offset:384
	s_waitcnt lgkmcnt(0)
	v_mfma_f32_32x32x16_bf16 v[36:51], v[188:191], v[136:139], v[36:51]
	ds_read_b128 v[188:191], v186 offset:416
	s_waitcnt lgkmcnt(0)
	v_mfma_f32_32x32x16_bf16 v[36:51], v[188:191], v[144:147], v[36:51]
	ds_read_b128 v[188:191], v186 offset:448
	s_waitcnt lgkmcnt(0)
	v_mfma_f32_32x32x16_bf16 v[36:51], v[188:191], v[140:143], v[36:51]
	ds_read_b128 v[188:191], v186 offset:480
	s_waitcnt lgkmcnt(0)
	v_mfma_f32_32x32x16_bf16 v[36:51], v[188:191], v[132:135], v[36:51]
	ds_read_b128 v[188:191], v184 offset:384
	s_waitcnt lgkmcnt(0)
	v_mfma_f32_32x32x16_bf16 v[20:35], v[188:191], v[136:139], v[20:35]
	ds_read_b128 v[188:191], v184 offset:416
	s_waitcnt lgkmcnt(0)
	v_mfma_f32_32x32x16_bf16 v[20:35], v[188:191], v[144:147], v[20:35]
	ds_read_b128 v[188:191], v184 offset:448
	s_waitcnt lgkmcnt(0)
	v_mfma_f32_32x32x16_bf16 v[20:35], v[188:191], v[140:143], v[20:35]
	ds_read_b128 v[188:191], v184 offset:480
	s_waitcnt lgkmcnt(0)
	v_mfma_f32_32x32x16_bf16 v[20:35], v[188:191], v[132:135], v[20:35]
	ds_read_b128 v[188:191], v187 offset:384
	s_waitcnt lgkmcnt(0)
	v_mfma_f32_32x32x16_bf16 v[4:19], v[188:191], v[136:139], v[4:19]
	ds_read_b128 v[136:139], v187 offset:416
	s_waitcnt lgkmcnt(0)
	v_mfma_f32_32x32x16_bf16 v[4:19], v[136:139], v[144:147], v[4:19]
	ds_read_b128 v[136:139], v187 offset:448
	s_waitcnt lgkmcnt(0)
	v_mfma_f32_32x32x16_bf16 v[4:19], v[136:139], v[140:143], v[4:19]
	ds_read_b128 v[136:139], v187 offset:480
	s_waitcnt lgkmcnt(0)
	s_barrier
	v_mfma_f32_32x32x16_bf16 v[4:19], v[136:139], v[132:135], v[4:19]
	v_max_f32_e32 v132, v117, v117
	v_max_f32_e32 v133, v116, v116
	v_max_f32_e32 v132, v133, v132
	v_max3_f32 v132, v132, v118, v119
	v_max3_f32 v132, v132, v120, v121
	v_max3_f32 v132, v132, v122, v123
	v_max3_f32 v132, v132, v124, v125
	v_max3_f32 v132, v132, v126, v127
	v_max3_f32 v132, v132, v128, v129
	v_max3_f32 v132, v132, v130, v131
	v_max3_f32 v132, v132, v100, v101
	v_max3_f32 v132, v132, v102, v103
	v_max3_f32 v132, v132, v104, v105
	v_max3_f32 v132, v132, v106, v107
	v_max3_f32 v132, v132, v108, v109
	v_max3_f32 v132, v132, v110, v111
	v_max3_f32 v132, v132, v112, v113
	v_max3_f32 v132, v132, v114, v115
	v_max3_f32 v132, v132, v84, v85
	v_max3_f32 v132, v132, v86, v87
	v_max3_f32 v132, v132, v88, v89
	v_max3_f32 v132, v132, v90, v91
	v_max3_f32 v132, v132, v92, v93
	v_max3_f32 v132, v132, v94, v95
	v_max3_f32 v132, v132, v96, v97
	v_max3_f32 v132, v132, v98, v99
	v_max3_f32 v132, v132, v68, v69
	v_max3_f32 v132, v132, v70, v71
	v_max3_f32 v132, v132, v72, v73
	v_max3_f32 v132, v132, v74, v75
	v_max3_f32 v132, v132, v76, v77
	v_max3_f32 v132, v132, v78, v79
	v_max3_f32 v132, v132, v80, v81
	v_max3_f32 v132, v132, v82, v83
	v_max3_f32 v132, v132, v52, v53
	v_max3_f32 v132, v132, v54, v55
	v_max3_f32 v132, v132, v56, v57
	v_max3_f32 v132, v132, v58, v59
	v_max3_f32 v132, v132, v60, v61
	v_max3_f32 v132, v132, v62, v63
	v_max3_f32 v132, v132, v64, v65
	v_max3_f32 v132, v132, v66, v67
	v_max3_f32 v132, v132, v36, v37
	v_max3_f32 v132, v132, v38, v39
	v_max3_f32 v132, v132, v40, v41
	v_max3_f32 v132, v132, v42, v43
	v_max3_f32 v132, v132, v44, v45
	v_max3_f32 v132, v132, v46, v47
	v_max3_f32 v132, v132, v48, v49
	v_max3_f32 v132, v132, v50, v51
	v_max3_f32 v132, v132, v20, v21
	v_max3_f32 v132, v132, v22, v23
	v_max3_f32 v132, v132, v24, v25
	v_max3_f32 v132, v132, v26, v27
	v_max3_f32 v132, v132, v28, v29
	v_max3_f32 v132, v132, v30, v31
	v_max3_f32 v132, v132, v32, v33
	v_max3_f32 v132, v132, v34, v35
	v_max3_f32 v132, v132, v4, v5
	v_max3_f32 v132, v132, v6, v7
	v_max3_f32 v132, v132, v8, v9
	v_max3_f32 v132, v132, v10, v11
	v_and_b32_e32 v134, 64, v250
	v_max3_f32 v132, v132, v12, v13
	v_xor_b32_e32 v133, 32, v250
	v_add_u32_e32 v134, 64, v134
	v_max3_f32 v132, v132, v14, v15
	v_cmp_lt_i32_e32 vcc, v133, v134
	v_max3_f32 v132, v132, v16, v17
	v_max3_f32 v132, v132, v18, v19
	v_cndmask_b32_e32 v133, v250, v133, vcc
	v_lshlrev_b32_e32 v134, 2, v133
	v_mov_b32_e32 v133, v132
	s_nop 3
	v_permlane32_swap_b32_e32 v132, v133
	s_nop 1
	s_waitcnt lgkmcnt(0)
	v_max_f32_e32 v133, v132, v133
	v_mov_b32_e32 v132, v19
	v_pk_mul_f32 v[132:133], v[172:173], v[132:133] op_sel_hi:[0,1]
	v_fma_f32 v19, v172, v116, -v133
	v_exp_f32_e32 v19, v19
	v_fma_f32 v116, v172, v117, -v133
	v_exp_f32_e32 v116, v116
	v_fma_f32 v117, v172, v118, -v133
	v_exp_f32_e32 v117, v117
	v_fma_f32 v118, v172, v119, -v133
	v_exp_f32_e32 v118, v118
	v_fma_f32 v119, v172, v120, -v133
	v_add_f32_e32 v135, 0, v19
	v_exp_f32_e32 v119, v119
	v_fma_f32 v120, v172, v121, -v133
	v_add_f32_e32 v135, v116, v135
	v_exp_f32_e32 v120, v120
	v_fma_f32 v121, v172, v122, -v133
	v_add_f32_e32 v135, v117, v135
	v_exp_f32_e32 v121, v121
	v_fma_f32 v122, v172, v123, -v133
	v_add_f32_e32 v135, v118, v135
	v_exp_f32_e32 v122, v122
	v_fma_f32 v123, v172, v124, -v133
	v_add_f32_e32 v135, v119, v135
	v_exp_f32_e32 v123, v123
	v_fma_f32 v124, v172, v125, -v133
	v_add_f32_e32 v135, v120, v135
	v_exp_f32_e32 v124, v124
	v_fma_f32 v125, v172, v126, -v133
	v_add_f32_e32 v135, v121, v135
	v_exp_f32_e32 v125, v125
	v_fma_f32 v126, v172, v127, -v133
	v_add_f32_e32 v135, v122, v135
	v_exp_f32_e32 v126, v126
	v_fma_f32 v127, v172, v128, -v133
	v_add_f32_e32 v135, v123, v135
	v_exp_f32_e32 v127, v127
	v_fma_f32 v128, v172, v129, -v133
	v_add_f32_e32 v135, v124, v135
	v_exp_f32_e32 v128, v128
	v_fma_f32 v129, v172, v130, -v133
	v_add_f32_e32 v135, v125, v135
	v_exp_f32_e32 v129, v129
	v_fma_f32 v130, v172, v131, -v133
	v_add_f32_e32 v135, v126, v135
	v_exp_f32_e32 v130, v130
	v_fma_f32 v100, v172, v100, -v133
	v_add_f32_e32 v135, v127, v135
	v_exp_f32_e32 v100, v100
	v_fma_f32 v101, v172, v101, -v133
	v_add_f32_e32 v135, v128, v135
	v_exp_f32_e32 v101, v101
	v_fma_f32 v102, v172, v102, -v133
	v_add_f32_e32 v135, v129, v135
	v_exp_f32_e32 v102, v102
	v_fma_f32 v103, v172, v103, -v133
	v_add_f32_e32 v131, v130, v135
	v_exp_f32_e32 v103, v103
	v_fma_f32 v104, v172, v104, -v133
	v_add_f32_e32 v131, v100, v131
	v_exp_f32_e32 v104, v104
	v_fma_f32 v105, v172, v105, -v133
	v_add_f32_e32 v131, v101, v131
	v_exp_f32_e32 v105, v105
	v_fma_f32 v106, v172, v106, -v133
	v_add_f32_e32 v131, v102, v131
	v_exp_f32_e32 v106, v106
	v_fma_f32 v107, v172, v107, -v133
	v_add_f32_e32 v131, v103, v131
	v_exp_f32_e32 v107, v107
	v_fma_f32 v108, v172, v108, -v133
	v_add_f32_e32 v131, v104, v131
	v_exp_f32_e32 v108, v108
	v_fma_f32 v109, v172, v109, -v133
	v_add_f32_e32 v131, v105, v131
	v_exp_f32_e32 v109, v109
	v_fma_f32 v110, v172, v110, -v133
	v_add_f32_e32 v131, v106, v131
	v_exp_f32_e32 v110, v110
	v_fma_f32 v111, v172, v111, -v133
	v_add_f32_e32 v131, v107, v131
	v_exp_f32_e32 v111, v111
	v_fma_f32 v112, v172, v112, -v133
	v_add_f32_e32 v131, v108, v131
	v_exp_f32_e32 v112, v112
	v_fma_f32 v113, v172, v113, -v133
	v_add_f32_e32 v131, v109, v131
	v_exp_f32_e32 v113, v113
	v_fma_f32 v114, v172, v114, -v133
	v_add_f32_e32 v131, v110, v131
	v_exp_f32_e32 v114, v114
	v_fma_f32 v115, v172, v115, -v133
	v_add_f32_e32 v131, v111, v131
	v_exp_f32_e32 v115, v115
	v_fma_f32 v84, v172, v84, -v133
	v_add_f32_e32 v131, v112, v131
	v_exp_f32_e32 v84, v84
	v_fma_f32 v85, v172, v85, -v133
	v_add_f32_e32 v131, v113, v131
	v_exp_f32_e32 v85, v85
	v_fma_f32 v86, v172, v86, -v133
	v_add_f32_e32 v131, v114, v131
	v_exp_f32_e32 v86, v86
	v_fma_f32 v87, v172, v87, -v133
	v_add_f32_e32 v131, v115, v131
	v_exp_f32_e32 v87, v87
	v_fma_f32 v88, v172, v88, -v133
	v_add_f32_e32 v131, v84, v131
	v_exp_f32_e32 v88, v88
	v_fma_f32 v89, v172, v89, -v133
	v_add_f32_e32 v131, v85, v131
	v_exp_f32_e32 v89, v89
	v_fma_f32 v90, v172, v90, -v133
	v_add_f32_e32 v131, v86, v131
	v_exp_f32_e32 v90, v90
	v_fma_f32 v91, v172, v91, -v133
	v_add_f32_e32 v131, v87, v131
	v_exp_f32_e32 v91, v91
	v_fma_f32 v92, v172, v92, -v133
	v_add_f32_e32 v131, v88, v131
	v_exp_f32_e32 v92, v92
	v_fma_f32 v93, v172, v93, -v133
	v_add_f32_e32 v131, v89, v131
	v_exp_f32_e32 v93, v93
	v_fma_f32 v94, v172, v94, -v133
	v_add_f32_e32 v131, v90, v131
	v_exp_f32_e32 v94, v94
	v_fma_f32 v95, v172, v95, -v133
	v_add_f32_e32 v131, v91, v131
	v_exp_f32_e32 v95, v95
	v_fma_f32 v96, v172, v96, -v133
	v_add_f32_e32 v131, v92, v131
	v_exp_f32_e32 v96, v96
	v_fma_f32 v97, v172, v97, -v133
	v_add_f32_e32 v131, v93, v131
	v_exp_f32_e32 v97, v97
	v_fma_f32 v98, v172, v98, -v133
	v_add_f32_e32 v131, v94, v131
	v_exp_f32_e32 v98, v98
	v_fma_f32 v99, v172, v99, -v133
	v_add_f32_e32 v131, v95, v131
	v_exp_f32_e32 v99, v99
	v_fma_f32 v68, v172, v68, -v133
	v_add_f32_e32 v131, v96, v131
	v_exp_f32_e32 v68, v68
	v_fma_f32 v69, v172, v69, -v133
	v_add_f32_e32 v131, v97, v131
	v_exp_f32_e32 v69, v69
	v_fma_f32 v70, v172, v70, -v133
	v_add_f32_e32 v131, v98, v131
	v_exp_f32_e32 v70, v70
	v_fma_f32 v71, v172, v71, -v133
	v_add_f32_e32 v131, v99, v131
	v_exp_f32_e32 v71, v71
	v_fma_f32 v72, v172, v72, -v133
	v_add_f32_e32 v131, v68, v131
	v_exp_f32_e32 v72, v72
	v_fma_f32 v73, v172, v73, -v133
	v_add_f32_e32 v131, v69, v131
	v_exp_f32_e32 v73, v73
	v_fma_f32 v74, v172, v74, -v133
	v_add_f32_e32 v131, v70, v131
	v_exp_f32_e32 v74, v74
	v_fma_f32 v75, v172, v75, -v133
	v_add_f32_e32 v131, v71, v131
	v_exp_f32_e32 v75, v75
	v_fma_f32 v76, v172, v76, -v133
	v_add_f32_e32 v131, v72, v131
	v_exp_f32_e32 v76, v76
	v_fma_f32 v77, v172, v77, -v133
	v_add_f32_e32 v131, v73, v131
	v_exp_f32_e32 v77, v77
	v_fma_f32 v78, v172, v78, -v133
	v_add_f32_e32 v131, v74, v131
	v_exp_f32_e32 v78, v78
	v_fma_f32 v79, v172, v79, -v133
	v_add_f32_e32 v131, v75, v131
	v_exp_f32_e32 v79, v79
	v_fma_f32 v80, v172, v80, -v133
	v_add_f32_e32 v131, v76, v131
	v_exp_f32_e32 v80, v80
	v_fma_f32 v81, v172, v81, -v133
	v_add_f32_e32 v131, v77, v131
	v_exp_f32_e32 v81, v81
	v_fma_f32 v82, v172, v82, -v133
	v_add_f32_e32 v131, v78, v131
	v_exp_f32_e32 v82, v82
	v_fma_f32 v83, v172, v83, -v133
	v_add_f32_e32 v131, v79, v131
	v_exp_f32_e32 v83, v83
	v_fma_f32 v52, v172, v52, -v133
	v_add_f32_e32 v131, v80, v131
	v_exp_f32_e32 v135, v52
	v_fma_f32 v53, v172, v53, -v133
	v_add_f32_e32 v131, v81, v131
	v_exp_f32_e32 v136, v53
	v_fma_f32 v53, v172, v54, -v133
	v_add_f32_e32 v131, v82, v131
	v_exp_f32_e32 v137, v53
	v_fma_f32 v53, v172, v55, -v133
	v_add_f32_e32 v131, v83, v131
	v_exp_f32_e32 v138, v53
	v_fma_f32 v53, v172, v56, -v133
	v_add_f32_e32 v52, v135, v131
	v_exp_f32_e32 v139, v53
	v_fma_f32 v53, v172, v57, -v133
	v_add_f32_e32 v52, v136, v52
	v_exp_f32_e32 v140, v53
	v_fma_f32 v53, v172, v58, -v133
	v_add_f32_e32 v52, v137, v52
	v_exp_f32_e32 v141, v53
	v_fma_f32 v53, v172, v59, -v133
	v_add_f32_e32 v52, v138, v52
	v_exp_f32_e32 v142, v53
	v_fma_f32 v53, v172, v60, -v133
	v_add_f32_e32 v52, v139, v52
	v_exp_f32_e32 v143, v53
	v_fma_f32 v53, v172, v61, -v133
	v_add_f32_e32 v52, v140, v52
	v_exp_f32_e32 v144, v53
	v_fma_f32 v53, v172, v62, -v133
	v_add_f32_e32 v52, v141, v52
	v_exp_f32_e32 v145, v53
	v_fma_f32 v53, v172, v63, -v133
	v_add_f32_e32 v52, v142, v52
	v_exp_f32_e32 v146, v53
	v_fma_f32 v53, v172, v64, -v133
	v_add_f32_e32 v52, v143, v52
	v_exp_f32_e32 v147, v53
	v_fma_f32 v53, v172, v65, -v133
	v_add_f32_e32 v52, v144, v52
	v_exp_f32_e32 v174, v53
	v_fma_f32 v53, v172, v66, -v133
	v_add_f32_e32 v52, v145, v52
	v_exp_f32_e32 v175, v53
	v_fma_f32 v53, v172, v67, -v133
	v_add_f32_e32 v52, v146, v52
	v_exp_f32_e32 v188, v53
	v_fma_f32 v36, v172, v36, -v133
	v_add_f32_e32 v52, v147, v52
	v_exp_f32_e32 v189, v36
	v_fma_f32 v37, v172, v37, -v133
	v_add_f32_e32 v52, v174, v52
	v_exp_f32_e32 v190, v37
	v_fma_f32 v37, v172, v38, -v133
	v_add_f32_e32 v52, v175, v52
	v_exp_f32_e32 v191, v37
	v_fma_f32 v37, v172, v39, -v133
	v_add_f32_e32 v52, v188, v52
	v_exp_f32_e32 v192, v37
	v_fma_f32 v37, v172, v40, -v133
	v_add_f32_e32 v36, v189, v52
	v_exp_f32_e32 v193, v37
	v_fma_f32 v37, v172, v41, -v133
	v_add_f32_e32 v36, v190, v36
	v_exp_f32_e32 v194, v37
	v_fma_f32 v37, v172, v42, -v133
	v_add_f32_e32 v36, v191, v36
	v_exp_f32_e32 v195, v37
	v_fma_f32 v37, v172, v43, -v133
	v_add_f32_e32 v36, v192, v36
	v_exp_f32_e32 v196, v37
	v_fma_f32 v37, v172, v44, -v133
	v_add_f32_e32 v36, v193, v36
	v_exp_f32_e32 v197, v37
	v_fma_f32 v37, v172, v45, -v133
	v_add_f32_e32 v36, v194, v36
	v_exp_f32_e32 v198, v37
	v_fma_f32 v37, v172, v46, -v133
	v_add_f32_e32 v36, v195, v36
	v_exp_f32_e32 v199, v37
	v_fma_f32 v37, v172, v47, -v133
	v_add_f32_e32 v36, v196, v36
	v_exp_f32_e32 v203, v37
	v_fma_f32 v37, v172, v48, -v133
	v_add_f32_e32 v36, v197, v36
	v_exp_f32_e32 v204, v37
	v_fma_f32 v37, v172, v49, -v133
	v_add_f32_e32 v36, v198, v36
	v_exp_f32_e32 v205, v37
	v_fma_f32 v37, v172, v50, -v133
	v_add_f32_e32 v36, v199, v36
	v_exp_f32_e32 v206, v37
	v_fma_f32 v37, v172, v51, -v133
	v_add_f32_e32 v36, v203, v36
	v_exp_f32_e32 v207, v37
	v_fma_f32 v20, v172, v20, -v133
	v_add_f32_e32 v36, v204, v36
	v_exp_f32_e32 v20, v20
	v_fma_f32 v21, v172, v21, -v133
	v_add_f32_e32 v36, v205, v36
	v_exp_f32_e32 v21, v21
	v_fma_f32 v22, v172, v22, -v133
	v_add_f32_e32 v36, v206, v36
	v_exp_f32_e32 v22, v22
	v_fma_f32 v23, v172, v23, -v133
	v_add_f32_e32 v36, v207, v36
	v_exp_f32_e32 v23, v23
	v_fma_f32 v24, v172, v24, -v133
	v_add_f32_e32 v36, v20, v36
	v_exp_f32_e32 v24, v24
	v_fma_f32 v25, v172, v25, -v133
	v_add_f32_e32 v36, v21, v36
	v_exp_f32_e32 v25, v25
	v_fma_f32 v26, v172, v26, -v133
	v_add_f32_e32 v36, v22, v36
	v_exp_f32_e32 v26, v26
	v_fma_f32 v27, v172, v27, -v133
	v_add_f32_e32 v36, v23, v36
	v_exp_f32_e32 v27, v27
	v_fma_f32 v28, v172, v28, -v133
	v_add_f32_e32 v36, v24, v36
	v_exp_f32_e32 v28, v28
	v_fma_f32 v29, v172, v29, -v133
	v_add_f32_e32 v36, v25, v36
	v_exp_f32_e32 v29, v29
	v_fma_f32 v30, v172, v30, -v133
	v_add_f32_e32 v36, v26, v36
	v_exp_f32_e32 v30, v30
	v_fma_f32 v31, v172, v31, -v133
	v_add_f32_e32 v36, v27, v36
	v_exp_f32_e32 v31, v31
	v_fma_f32 v32, v172, v32, -v133
	v_add_f32_e32 v36, v28, v36
	v_exp_f32_e32 v32, v32
	v_fma_f32 v33, v172, v33, -v133
	v_add_f32_e32 v36, v29, v36
	v_exp_f32_e32 v33, v33
	v_fma_f32 v34, v172, v34, -v133
	v_add_f32_e32 v36, v30, v36
	v_exp_f32_e32 v34, v34
	v_fma_f32 v35, v172, v35, -v133
	v_add_f32_e32 v36, v31, v36
	v_exp_f32_e32 v35, v35
	v_fma_f32 v4, v172, v4, -v133
	v_add_f32_e32 v36, v32, v36
	v_exp_f32_e32 v4, v4
	v_fma_f32 v5, v172, v5, -v133
	v_add_f32_e32 v36, v33, v36
	v_exp_f32_e32 v5, v5
	v_fma_f32 v6, v172, v6, -v133
	v_add_f32_e32 v36, v34, v36
	v_exp_f32_e32 v6, v6
	v_fma_f32 v7, v172, v7, -v133
	v_add_f32_e32 v36, v35, v36
	v_exp_f32_e32 v7, v7
	v_fma_f32 v8, v172, v8, -v133
	v_add_f32_e32 v36, v4, v36
	v_exp_f32_e32 v8, v8
	v_fma_f32 v9, v172, v9, -v133
	v_add_f32_e32 v36, v5, v36
	v_exp_f32_e32 v9, v9
	v_fma_f32 v10, v172, v10, -v133
	v_add_f32_e32 v36, v6, v36
	v_exp_f32_e32 v10, v10
	v_fma_f32 v11, v172, v11, -v133
	v_add_f32_e32 v36, v7, v36
	v_exp_f32_e32 v11, v11
	v_fma_f32 v12, v172, v12, -v133
	v_add_f32_e32 v36, v8, v36
	v_exp_f32_e32 v12, v12
	v_fma_f32 v13, v172, v13, -v133
	v_add_f32_e32 v36, v9, v36
	v_exp_f32_e32 v13, v13
	v_fma_f32 v14, v172, v14, -v133
	v_add_f32_e32 v36, v10, v36
	v_exp_f32_e32 v14, v14
	v_fma_f32 v15, v172, v15, -v133
	v_add_f32_e32 v36, v11, v36
	v_exp_f32_e32 v15, v15
	v_fma_f32 v16, v172, v16, -v133
	v_add_f32_e32 v36, v12, v36
	v_exp_f32_e32 v16, v16
	v_fma_f32 v17, v172, v17, -v133
	v_add_f32_e32 v36, v13, v36
	v_exp_f32_e32 v17, v17
	v_fma_f32 v18, v172, v18, -v133
	v_add_f32_e32 v36, v14, v36
	v_exp_f32_e32 v18, v18
	v_sub_f32_e32 v37, v132, v133
	v_add_f32_e32 v36, v15, v36
	v_exp_f32_e32 v132, v37
	v_add_f32_e32 v36, v16, v36
	v_add_f32_e32 v36, v17, v36
	v_add_f32_e32 v36, v18, v36
	v_add_f32_e32 v36, v132, v36
	v_mov_b32_e32 v37, v36
	s_nop 3
	v_permlane32_swap_b32_e32 v36, v37
	s_nop 1
	v_cvt_pk_bf16_f32 v59, v98, v99
	v_cvt_pk_bf16_f32 v98, v16, v17
	v_lshl_add_u64 v[16:17], v[158:159], 0, s[12:13]
	v_cvt_pk_bf16_f32 v56, v92, v93
	v_cvt_pk_bf16_f32 v92, v4, v5
	v_lshl_add_u64 v[4:5], v[16:17], 0, v[160:161]
	s_or_b32 s12, s4, 64
	v_cvt_pk_bf16_f32 v57, v94, v95
	v_cvt_pk_bf16_f32 v93, v6, v7
	v_cvt_pk_bf16_f32 v94, v8, v9
	global_load_dwordx4 v[4:7], v[4:5], off
	v_lshl_add_u64 v[8:9], v[16:17], 0, v[162:163]
	s_ashr_i32 s13, s12, 31
	v_cvt_pk_bf16_f32 v58, v96, v97
	v_cvt_pk_bf16_f32 v95, v10, v11
	v_cvt_pk_bf16_f32 v96, v12, v13
	global_load_dwordx4 v[8:11], v[8:9], off
	v_lshl_add_u64 v[12:13], v[16:17], 0, v[164:165]
	s_lshl_b64 s[12:13], s[12:13], 9
	v_cvt_pk_bf16_f32 v55, v90, v91
	v_cvt_pk_bf16_f32 v90, v32, v33
	v_cvt_pk_bf16_f32 v97, v14, v15
	global_load_dwordx4 v[12:15], v[12:13], off
	v_lshl_add_u64 v[16:17], v[16:17], 0, v[166:167]
	v_lshl_add_u64 v[32:33], v[158:159], 0, s[12:13]
	s_waitcnt lgkmcnt(0)
	v_add_f32_e32 v131, v36, v37
	v_cvt_pk_bf16_f32 v36, v19, v116
	v_cvt_pk_bf16_f32 v52, v84, v85
	v_cvt_pk_bf16_f32 v84, v20, v21
	v_cvt_pk_bf16_f32 v99, v18, v132
	global_load_dwordx4 v[16:19], v[16:17], off
	v_lshl_add_u64 v[20:21], v[32:33], 0, v[160:161]
	v_cvt_pk_bf16_f32 v53, v86, v87
	v_cvt_pk_bf16_f32 v85, v22, v23
	v_cvt_pk_bf16_f32 v86, v24, v25
	global_load_dwordx4 v[20:23], v[20:21], off
	v_lshl_add_u64 v[24:25], v[32:33], 0, v[162:163]
	v_cvt_pk_bf16_f32 v54, v88, v89
	v_cvt_pk_bf16_f32 v87, v26, v27
	v_cvt_pk_bf16_f32 v88, v28, v29
	global_load_dwordx4 v[24:27], v[24:25], off
	v_lshl_add_u64 v[28:29], v[32:33], 0, v[164:165]
	v_cvt_pk_bf16_f32 v89, v30, v31
	global_load_dwordx4 v[28:31], v[28:29], off
	v_lshl_add_u64 v[32:33], v[32:33], 0, v[166:167]
	v_cvt_pk_bf16_f32 v91, v34, v35
	global_load_dwordx4 v[32:35], v[32:33], off
	s_or_b32 s12, s4, 0x80
	s_ashr_i32 s13, s12, 31
	s_lshl_b64 s[12:13], s[12:13], 9
	s_waitcnt vmcnt(7)
	ds_write_b128 v179, v[4:7]
	s_waitcnt vmcnt(6)
	ds_write_b128 v179, v[8:11] offset:8448
	s_waitcnt vmcnt(5)
	ds_write_b128 v179, v[12:15] offset:16896
	s_waitcnt vmcnt(4)
	ds_write_b128 v179, v[16:19] offset:25344
	s_waitcnt vmcnt(3)
	ds_write_b128 v179, v[20:23] offset:33792
	s_waitcnt vmcnt(2)
	ds_write_b128 v179, v[24:27] offset:42240
	s_waitcnt vmcnt(1)
	ds_write_b128 v179, v[28:31] offset:50688
	s_waitcnt vmcnt(0)
	ds_write_b128 v179, v[32:35] offset:59136
	v_lshl_add_u64 v[16:17], v[158:159], 0, s[12:13]
	v_lshl_add_u64 v[4:5], v[16:17], 0, v[160:161]
	s_or_b32 s4, s4, 0xc0
	global_load_dwordx4 v[4:7], v[4:5], off
	v_lshl_add_u64 v[8:9], v[16:17], 0, v[162:163]
	s_ashr_i32 s5, s4, 31
	global_load_dwordx4 v[8:11], v[8:9], off
	v_lshl_add_u64 v[12:13], v[16:17], 0, v[164:165]
	s_lshl_b64 s[4:5], s[4:5], 9
	global_load_dwordx4 v[12:15], v[12:13], off
	v_lshl_add_u64 v[16:17], v[16:17], 0, v[166:167]
	v_lshl_add_u64 v[32:33], v[158:159], 0, s[4:5]
	global_load_dwordx4 v[16:19], v[16:17], off
	v_lshl_add_u64 v[20:21], v[32:33], 0, v[160:161]
	global_load_dwordx4 v[20:23], v[20:21], off
	v_lshl_add_u64 v[24:25], v[32:33], 0, v[162:163]
	global_load_dwordx4 v[24:27], v[24:25], off
	v_lshl_add_u64 v[28:29], v[32:33], 0, v[164:165]
	global_load_dwordx4 v[28:31], v[28:29], off
	v_lshl_add_u64 v[32:33], v[32:33], 0, v[166:167]
	global_load_dwordx4 v[32:35], v[32:33], off
	s_waitcnt vmcnt(7)
	ds_write_b128 v180, v[4:7]
	s_waitcnt vmcnt(6)
	ds_write_b128 v180, v[8:11] offset:8448
	s_waitcnt vmcnt(5)
	ds_write_b128 v180, v[12:15] offset:16896
	s_waitcnt vmcnt(4)
	ds_write_b128 v180, v[16:19] offset:25344
	s_waitcnt vmcnt(3)
	ds_write_b128 v181, v[20:23]
	s_waitcnt vmcnt(2)
	ds_write_b128 v181, v[24:27] offset:8448
	s_waitcnt vmcnt(1)
	ds_write_b128 v181, v[28:31] offset:16896
	s_waitcnt vmcnt(0)
	ds_write_b128 v181, v[32:35] offset:25344
	v_div_scale_f32 v4, s[4:5], v131, v131, 1.0
	v_rcp_f32_e32 v5, v4
	v_cvt_pk_bf16_f32 v44, v100, v101
	v_cvt_pk_bf16_f32 v37, v117, v118
	v_cvt_pk_bf16_f32 v38, v119, v120
	v_fma_f32 v6, -v4, v5, 1.0
	v_fmac_f32_e32 v5, v6, v5
	v_div_scale_f32 v6, vcc, 1.0, v131, 1.0
	v_mul_f32_e32 v7, v6, v5
	v_fma_f32 v8, -v4, v7, v6
	v_fmac_f32_e32 v7, v8, v5
	v_fma_f32 v4, -v4, v7, v6
	v_div_fmas_f32 v4, v4, v5, v7
	v_div_fixup_f32 v100, v4, v131, 1.0
	v_lshl_add_u64 v[4:5], v[170:171], 0, s[18:19]
	v_cvt_pk_bf16_f32 v39, v121, v122
	v_cvt_pk_bf16_f32 v40, v123, v124
	v_cvt_pk_bf16_f32 v41, v125, v126
	v_cvt_pk_bf16_f32 v42, v127, v128
	v_cvt_pk_bf16_f32 v43, v129, v130
	v_cvt_pk_bf16_f32 v45, v102, v103
	v_cvt_pk_bf16_f32 v46, v104, v105
	v_cvt_pk_bf16_f32 v47, v106, v107
	v_cvt_pk_bf16_f32 v48, v108, v109
	v_cvt_pk_bf16_f32 v49, v110, v111
	v_cvt_pk_bf16_f32 v50, v112, v113
	v_cvt_pk_bf16_f32 v51, v114, v115
	v_cvt_pk_bf16_f32 v60, v68, v69
	v_cvt_pk_bf16_f32 v61, v70, v71
	v_cvt_pk_bf16_f32 v62, v72, v73
	v_cvt_pk_bf16_f32 v63, v74, v75
	v_cvt_pk_bf16_f32 v64, v76, v77
	v_cvt_pk_bf16_f32 v65, v78, v79
	v_cvt_pk_bf16_f32 v66, v80, v81
	v_cvt_pk_bf16_f32 v67, v82, v83
	v_cvt_pk_bf16_f32 v68, v135, v136
	v_cvt_pk_bf16_f32 v69, v137, v138
	v_cvt_pk_bf16_f32 v70, v139, v140
	v_cvt_pk_bf16_f32 v71, v141, v142
	v_cvt_pk_bf16_f32 v72, v143, v144
	v_cvt_pk_bf16_f32 v73, v145, v146
	v_cvt_pk_bf16_f32 v74, v147, v174
	v_cvt_pk_bf16_f32 v75, v175, v188
	v_cvt_pk_bf16_f32 v76, v189, v190
	v_cvt_pk_bf16_f32 v77, v191, v192
	v_cvt_pk_bf16_f32 v78, v193, v194
	v_cvt_pk_bf16_f32 v79, v195, v196
	v_cvt_pk_bf16_f32 v80, v197, v198
	v_cvt_pk_bf16_f32 v81, v199, v203
	v_cvt_pk_bf16_f32 v82, v204, v205
	v_cvt_pk_bf16_f32 v83, v206, v207
	v_mov_b32_e32 v101, v100
	v_lshl_add_u64 v[102:103], v[168:169], 0, v[4:5]
	s_waitcnt lgkmcnt(0)
	s_barrier
